# speedup vs baseline: 1.0061x; 1.0061x over previous
.LBB0_23:
	s_andn2_b64 vcc, exec, s[4:5]
	s_cbranch_vccnz .LBB0_43
	s_load_dwordx2 s[4:5], s[0:1], 0x0
	s_add_i32 s3, s2, 0xfffffdd6
	s_ashr_i32 s76, s3, 4
	v_lshlrev_b32_e32 v43, 3, v31
	v_lshl_or_b32 v2, s76, 5, v43
	v_lshrrev_b32_e32 v42, 8, v0
	s_lshl_b32 s3, s3, 1
	v_ashrrev_i32_e32 v3, 31, v2
	v_and_or_b32 v1, s3, 30, v42
	v_lshlrev_b64 v[2:3], 15, v[2:3]
	s_waitcnt lgkmcnt(0)
	v_lshl_add_u64 v[2:3], s[4:5], 0, v[2:3]
	v_lshlrev_b32_e32 v38, 10, v1
	v_mov_b32_e32 v39, 0
	v_lshl_add_u64 v[2:3], v[2:3], 0, v[38:39]
	v_lshlrev_b32_e32 v38, 4, v30
	v_lshl_add_u64 v[2:3], v[2:3], 0, v[38:39]
	s_mov_b32 s3, 0x8000
	v_add_co_u32_e32 v4, vcc, s3, v2
	s_mov_b32 s3, 0x10000
	s_nop 0
	v_addc_co_u32_e32 v5, vcc, 0, v3, vcc
	global_load_dwordx4 v[34:37], v[2:3], off nt
	global_load_dwordx4 v[26:29], v[4:5], off nt
	v_add_co_u32_e32 v4, vcc, s3, v2
	s_mov_b32 s3, 0x18000
	s_nop 0
	v_addc_co_u32_e32 v5, vcc, 0, v3, vcc
	v_add_co_u32_e32 v6, vcc, s3, v2
	s_mov_b32 s3, 0x20000
	s_nop 0
	v_addc_co_u32_e32 v7, vcc, 0, v3, vcc
	global_load_dwordx4 v[22:25], v[4:5], off nt
	global_load_dwordx4 v[18:21], v[6:7], off nt
	v_add_co_u32_e32 v4, vcc, s3, v2
	s_mov_b32 s3, 0x28000
	s_nop 0
	v_addc_co_u32_e32 v5, vcc, 0, v3, vcc
	v_add_co_u32_e32 v6, vcc, s3, v2
	s_mov_b32 s3, 0x30000
	s_nop 0
	v_addc_co_u32_e32 v7, vcc, 0, v3, vcc
	v_add_co_u32_e32 v32, vcc, s3, v2
	s_mov_b32 s3, 0x38000
	s_nop 0
	v_addc_co_u32_e32 v33, vcc, 0, v3, vcc
	v_add_co_u32_e32 v40, vcc, s3, v2
	global_load_dwordx4 v[14:17], v[4:5], off nt
	global_load_dwordx4 v[10:13], v[6:7], off nt
	v_addc_co_u32_e32 v41, vcc, 0, v3, vcc
	global_load_dwordx4 v[6:9], v[32:33], off nt
	global_load_dwordx4 v[2:5], v[40:41], off nt
	v_mbcnt_lo_u32_b32 v33, -1, 0
	v_mbcnt_hi_u32_b32 v33, -1, v33
	v_and_b32_e32 v40, 64, v33
	v_xor_b32_e32 v39, 1, v33
	v_add_u32_e32 v40, 64, v40
	v_cmp_lt_i32_e32 vcc, v39, v40
	v_mov_b32_e32 v32, 0x800
	v_lshl_or_b32 v32, v42, 10, v32
	v_cndmask_b32_e32 v33, v33, v39, vcc
	v_lshlrev_b32_e32 v33, 2, v33
	s_waitcnt vmcnt(7)
	v_cmp_neq_f32_e32 vcc, 0, v34
	s_nop 1
	v_cndmask_b32_e64 v34, 0, 1, vcc
	v_cmp_neq_f32_e32 vcc, 0, v35
	s_nop 1
	v_cndmask_b32_e64 v35, 0, 2, vcc
	v_cmp_neq_f32_e32 vcc, 0, v36
	v_or_b32_e32 v34, v35, v34
	s_nop 0
	v_cndmask_b32_e64 v36, 0, 4, vcc
	v_cmp_neq_f32_e32 vcc, 0, v37
	s_nop 1
	v_cndmask_b32_e64 v35, 0, 8, vcc
	v_or3_b32 v35, v34, v36, v35
	s_nop 1
	v_mov_b32_dpp v36, v35 quad_perm:[1,0,3,2] row_mask:0xf bank_mask:0xf
	v_and_b32_e32 v34, 1, v0
	v_cmp_eq_u32_e32 vcc, 0, v34
	v_or_b32_e32 v34, v32, v43
	v_add_u32_e32 v34, v34, v38
	s_and_saveexec_b64 s[4:5], vcc
	s_cbranch_execz .LBB0_26
	v_lshl_or_b32 v35, v36, 4, v35
	ds_write_b8 v34, v35
.LBB0_26:
	s_or_b64 exec, exec, s[4:5]
	s_waitcnt vmcnt(6)
	v_cmp_neq_f32_e64 s[4:5], 0, v26
	s_nop 1
	v_cndmask_b32_e64 v26, 0, 1, s[4:5]
	v_cmp_neq_f32_e64 s[4:5], 0, v27
	s_nop 1
	v_cndmask_b32_e64 v27, 0, 2, s[4:5]
	v_cmp_neq_f32_e64 s[4:5], 0, v28
	v_or_b32_e32 v26, v27, v26
	s_nop 0
	v_cndmask_b32_e64 v27, 0, 4, s[4:5]
	v_cmp_neq_f32_e64 s[4:5], 0, v29
	s_nop 1
	v_cndmask_b32_e64 v28, 0, 8, s[4:5]
	v_or3_b32 v26, v26, v27, v28
	s_nop 1
	v_mov_b32_dpp v27, v26 quad_perm:[1,0,3,2] row_mask:0xf bank_mask:0xf
	s_and_saveexec_b64 s[4:5], vcc
	s_cbranch_execz .LBB0_28
	v_lshl_or_b32 v26, v27, 4, v26
	ds_write_b8 v34, v26 offset:1
.LBB0_28:
	s_or_b64 exec, exec, s[4:5]
	s_waitcnt vmcnt(5)
	v_cmp_neq_f32_e64 s[4:5], 0, v22
	s_nop 1
	v_cndmask_b32_e64 v22, 0, 1, s[4:5]
	v_cmp_neq_f32_e64 s[4:5], 0, v23
	s_nop 1
	v_cndmask_b32_e64 v23, 0, 2, s[4:5]
	v_cmp_neq_f32_e64 s[4:5], 0, v24
	v_or_b32_e32 v22, v23, v22
	s_nop 0
	v_cndmask_b32_e64 v23, 0, 4, s[4:5]
	v_cmp_neq_f32_e64 s[4:5], 0, v25
	s_nop 1
	v_cndmask_b32_e64 v24, 0, 8, s[4:5]
	v_or3_b32 v22, v22, v23, v24
	s_nop 1
	v_mov_b32_dpp v23, v22 quad_perm:[1,0,3,2] row_mask:0xf bank_mask:0xf
	s_and_saveexec_b64 s[4:5], vcc
	s_cbranch_execz .LBB0_30
	v_lshl_or_b32 v22, v23, 4, v22
	ds_write_b8 v34, v22 offset:2
.LBB0_30:
	s_or_b64 exec, exec, s[4:5]
	s_waitcnt vmcnt(4)
	v_cmp_neq_f32_e64 s[4:5], 0, v18
	s_nop 1
	v_cndmask_b32_e64 v18, 0, 1, s[4:5]
	v_cmp_neq_f32_e64 s[4:5], 0, v19
	s_nop 1
	v_cndmask_b32_e64 v19, 0, 2, s[4:5]
	v_cmp_neq_f32_e64 s[4:5], 0, v20
	v_or_b32_e32 v18, v19, v18
	s_nop 0
	v_cndmask_b32_e64 v19, 0, 4, s[4:5]
	v_cmp_neq_f32_e64 s[4:5], 0, v21
	s_nop 1
	v_cndmask_b32_e64 v20, 0, 8, s[4:5]
	v_or3_b32 v18, v18, v19, v20
	s_nop 1
	v_mov_b32_dpp v19, v18 quad_perm:[1,0,3,2] row_mask:0xf bank_mask:0xf
	s_and_saveexec_b64 s[4:5], vcc
	s_cbranch_execz .LBB0_32
	v_lshl_or_b32 v18, v19, 4, v18
	ds_write_b8 v34, v18 offset:3
.LBB0_32:
	s_or_b64 exec, exec, s[4:5]
	s_waitcnt vmcnt(3)
	v_cmp_neq_f32_e64 s[4:5], 0, v14
	s_nop 1
	v_cndmask_b32_e64 v14, 0, 1, s[4:5]
	v_cmp_neq_f32_e64 s[4:5], 0, v15
	s_nop 1
	v_cndmask_b32_e64 v15, 0, 2, s[4:5]
	v_cmp_neq_f32_e64 s[4:5], 0, v16
	v_or_b32_e32 v14, v15, v14
	s_nop 0
	v_cndmask_b32_e64 v15, 0, 4, s[4:5]
	v_cmp_neq_f32_e64 s[4:5], 0, v17
	s_nop 1
	v_cndmask_b32_e64 v16, 0, 8, s[4:5]
	v_or3_b32 v14, v14, v15, v16
	s_nop 1
	v_mov_b32_dpp v15, v14 quad_perm:[1,0,3,2] row_mask:0xf bank_mask:0xf
	s_and_saveexec_b64 s[4:5], vcc
	s_cbranch_execz .LBB0_34
	v_lshl_or_b32 v14, v15, 4, v14
	ds_write_b8 v34, v14 offset:4
.LBB0_34:
	s_or_b64 exec, exec, s[4:5]
	s_waitcnt vmcnt(2)
	v_cmp_neq_f32_e64 s[4:5], 0, v10
	s_nop 1
	v_cndmask_b32_e64 v10, 0, 1, s[4:5]
	v_cmp_neq_f32_e64 s[4:5], 0, v11
	s_nop 1
	v_cndmask_b32_e64 v11, 0, 2, s[4:5]
	v_cmp_neq_f32_e64 s[4:5], 0, v12
	v_or_b32_e32 v10, v11, v10
	s_nop 0
	v_cndmask_b32_e64 v11, 0, 4, s[4:5]
	v_cmp_neq_f32_e64 s[4:5], 0, v13
	s_nop 1
	v_cndmask_b32_e64 v12, 0, 8, s[4:5]
	v_or3_b32 v10, v10, v11, v12
	s_nop 1
	v_mov_b32_dpp v11, v10 quad_perm:[1,0,3,2] row_mask:0xf bank_mask:0xf
	s_and_saveexec_b64 s[4:5], vcc
	s_cbranch_execz .LBB0_36
	v_lshl_or_b32 v10, v11, 4, v10
	ds_write_b8 v34, v10 offset:5
.LBB0_36:
	s_or_b64 exec, exec, s[4:5]
	s_waitcnt vmcnt(1)
	v_cmp_neq_f32_e64 s[4:5], 0, v6
	s_nop 1
	v_cndmask_b32_e64 v6, 0, 1, s[4:5]
	v_cmp_neq_f32_e64 s[4:5], 0, v7
	s_nop 1
	v_cndmask_b32_e64 v7, 0, 2, s[4:5]
	v_cmp_neq_f32_e64 s[4:5], 0, v8
	v_or_b32_e32 v6, v7, v6
	s_nop 0
	v_cndmask_b32_e64 v7, 0, 4, s[4:5]
	v_cmp_neq_f32_e64 s[4:5], 0, v9
	s_nop 1
	v_cndmask_b32_e64 v8, 0, 8, s[4:5]
	v_or3_b32 v6, v6, v7, v8
	s_nop 1
	v_mov_b32_dpp v7, v6 quad_perm:[1,0,3,2] row_mask:0xf bank_mask:0xf
	s_and_saveexec_b64 s[4:5], vcc
	s_cbranch_execz .LBB0_38
	v_lshl_or_b32 v6, v7, 4, v6
	ds_write_b8 v34, v6 offset:6
.LBB0_38:
	s_or_b64 exec, exec, s[4:5]
	s_waitcnt vmcnt(0)
	v_cmp_neq_f32_e64 s[4:5], 0, v2
	s_nop 1
	v_cndmask_b32_e64 v2, 0, 1, s[4:5]
	v_cmp_neq_f32_e64 s[4:5], 0, v3
	s_nop 1
	v_cndmask_b32_e64 v3, 0, 2, s[4:5]
	v_cmp_neq_f32_e64 s[4:5], 0, v4
	v_or_b32_e32 v2, v3, v2
	s_nop 0
	v_cndmask_b32_e64 v3, 0, 4, s[4:5]
	v_cmp_neq_f32_e64 s[4:5], 0, v5
	s_nop 1
	v_cndmask_b32_e64 v4, 0, 8, s[4:5]
	v_or3_b32 v2, v2, v3, v4
	s_nop 1
	v_mov_b32_dpp v3, v2 quad_perm:[1,0,3,2] row_mask:0xf bank_mask:0xf
	s_and_saveexec_b64 s[4:5], vcc
	s_cbranch_execz .LBB0_40
	v_lshl_or_b32 v2, v3, 4, v2
	ds_write_b8 v34, v2 offset:7
